# speedup vs baseline: 1.0093x; 1.0093x over previous
_Z11attn_kernelPKDF16_S0_PDF16_:
	s_load_dwordx4 s[4:7], s[0:1], 0x0
	s_load_dwordx2 s[8:9], s[0:1], 0x10
	s_lshr_b32 s1, s2, 3
	s_lshr_b32 s10, s2, 7
	s_and_b32 s0, s2, 4
	s_and_b32 s1, s1, 8
	s_and_b32 s20, s2, 3
	s_lshl_b32 s30, s10, 4
	s_or_b32 s22, s1, s0
	s_or_b32 s0, s30, s20
	s_or_b32 s14, s0, s22
	s_or_b32 s0, s20, 16
	s_sub_i32 s0, s0, s30
	s_mov_b32 s15, 0
	s_or_b32 s0, s0, s22
	s_bfe_u32 s24, s2, 0x30003
	s_ashr_i32 s1, s0, 31
	s_lshl_b64 s[2:3], s[14:15], 18
	s_waitcnt lgkmcnt(0)
	s_add_u32 s2, s4, s2
	s_addc_u32 s3, s5, s3
	s_lshl_b64 s[0:1], s[0:1], 18
	s_add_u32 s11, s4, s0
	s_addc_u32 s12, s5, s1
	s_add_u32 s13, s6, s0
	v_readfirstlane_b32 s16, v0
	s_addc_u32 s18, s7, s1
	s_lshl_b32 s0, s24, 2
	s_lshr_b32 s1, s16, 7
	s_add_i32 s14, s1, s0
	s_lshr_b32 s23, s16, 6
	s_lshl_b64 s[0:1], s[14:15], 13
	s_add_u32 s0, s2, s0
	v_and_b32_e32 v189, 31, v0
	s_addc_u32 s1, s3, s1
	s_lshl_b32 s21, s23, 5
	v_and_or_b32 v1, s21, 32, v189
	v_lshlrev_b32_e32 v186, 4, v1
	v_mov_b32_e32 v187, 0
	s_lshl_b32 s14, s23, 9
	v_lshl_add_u64 v[2:3], s[0:1], 0, v[186:187]
	s_and_b32 s0, s16, 0x3fffffc0
	s_lshl_b64 s[16:17], s[14:15], 1
	v_and_b32_e32 v188, 63, v0
	s_add_u32 s2, s11, s16
	s_addc_u32 s3, s12, s17
	s_add_u32 s44, s2, 0x8000
	s_addc_u32 s45, s3, 0
	v_lshlrev_b32_e32 v186, 4, v188
	v_lshl_add_u64 v[44:45], s[2:3], 0, v[186:187]
	s_add_u32 s2, s13, s16
	s_addc_u32 s3, s18, s17
	s_add_u32 s46, s2, 0x6000
	s_addc_u32 s47, s3, 0
	s_lshl_b32 s25, s23, 10
	s_cmp_lg_u32 0, -1
	s_cselect_b32 s1, 0, 0
	v_bfe_u32 v46, v0, 5, 1
	s_add_i32 s25, s25, s1
	s_mov_b32 s1, m0
	s_mov_b32 m0, s25
	s_nop 0
	global_load_lds_dwordx4 v[44:45], off
	s_mov_b32 m0, s1
	v_lshl_add_u64 v[34:35], s[2:3], 0, v[186:187]
	s_add_i32 s26, s25, 0x6000
	v_lshlrev_b32_e32 v4, 10, v46
	s_mov_b32 s1, m0
	s_mov_b32 m0, s26
	s_nop 0
	global_load_lds_dwordx4 v[34:35], off
	s_mov_b32 m0, s1
	s_mov_b64 s[18:19], 0x2000
	v_mov_b32_e32 v5, v187
	v_lshl_add_u64 v[6:7], v[44:45], 0, s[18:19]
	s_add_i32 s1, s25, 0x2000
	s_mov_b32 s2, m0
	s_mov_b32 m0, s1
	s_nop 0
	global_load_lds_dwordx4 v[6:7], off
	s_mov_b32 m0, s2
	v_lshl_add_u64 v[2:3], v[2:3], 0, v[4:5]
	global_load_dwordx4 v[136:139], v[2:3], off
	global_load_dwordx4 v[128:131], v[2:3], off offset:2048
	s_movk_i32 s1, 0x1000
	v_add_co_u32_e32 v2, vcc, s1, v2
	v_lshlrev_b32_e32 v1, 4, v189
	s_nop 0
	v_addc_co_u32_e32 v3, vcc, 0, v3, vcc
	global_load_dwordx4 v[120:123], v[2:3], off
	global_load_dwordx4 v[112:115], v[2:3], off offset:2048
	v_add3_u32 v195, 0, v4, v1
	v_mov_b32_e32 v2, v187
	v_mov_b32_e32 v3, v187
	v_mov_b32_e32 v4, v187
	v_mov_b32_e32 v6, v187
	v_mov_b32_e32 v7, v187
	v_mov_b32_e32 v8, v187
	v_mov_b32_e32 v9, v187
	v_mov_b32_e32 v10, v187
	v_mov_b32_e32 v11, v187
	v_mov_b32_e32 v12, v187
	v_mov_b32_e32 v13, v187
	v_mov_b32_e32 v14, v187
	v_mov_b32_e32 v15, v187
	v_mov_b32_e32 v16, v187
	v_mov_b32_e32 v17, v187
	s_mov_b64 s[2:3], 0x4000
	v_lshl_add_u64 v[18:19], v[44:45], 0, s[2:3]
	s_add_i32 s1, s25, 0x4000
	s_mov_b32 s11, m0
	s_mov_b32 m0, s1
	s_nop 0
	global_load_lds_dwordx4 v[18:19], off
	s_mov_b32 m0, s11
	v_lshl_add_u64 v[18:19], v[34:35], 0, s[18:19]
	s_add_i32 s1, s25, 0x8000
	s_mov_b32 s11, m0
	s_mov_b32 m0, s1
	s_nop 0
	global_load_lds_dwordx4 v[18:19], off
	s_mov_b32 m0, s11
	s_waitcnt vmcnt(4) lgkmcnt(0)
	s_barrier
	ds_read_b128 v[36:39], v195
	ds_read_b128 v[40:43], v195 offset:512
	v_lshlrev_b32_e32 v190, 3, v0
	s_mov_b64 s[12:13], 0x6000
	s_or_b32 s14, s22, s20
	s_sub_i32 s14, s14, s30
	s_add_i32 s34, s14, 16
	s_lshl_b32 s0, s0, 2
	s_ashr_i32 s35, s34, 31
	s_lshl_b64 s[34:35], s[34:35], 18
	s_mov_b32 s27, -1
	s_waitcnt vmcnt(3) lgkmcnt(1)
	v_mfma_f32_32x32x16_f16 v[18:33], v[36:39], v[136:139], v[2:17]
	s_movk_i32 s28, 0x6000
	s_movk_i32 s31, 0x2000
	s_movk_i32 s29, 0x4000
	v_lshlrev_b32_e32 v191, 9, v46
	v_lshlrev_b32_e32 v193, 4, v46
	v_lshlrev_b32_e32 v180, 4, v188
	s_waitcnt lgkmcnt(0)
	v_mfma_f32_32x32x16_f16 v[2:17], v[40:43], v[136:139], v[2:17]
	ds_read_b128 v[36:39], v195 offset:2048
	ds_read_b128 v[40:43], v195 offset:2560
	s_waitcnt vmcnt(2) lgkmcnt(1)
	v_mfma_f32_32x32x16_f16 v[18:33], v[36:39], v[128:131], v[18:33]
	s_waitcnt lgkmcnt(0)
	v_mfma_f32_32x32x16_f16 v[2:17], v[40:43], v[128:131], v[2:17]
	ds_read_b128 v[36:39], v195 offset:4096
	ds_read_b128 v[40:43], v195 offset:4608
	s_waitcnt vmcnt(1) lgkmcnt(1)
	v_mfma_f32_32x32x16_f16 v[18:33], v[36:39], v[120:123], v[18:33]
	s_waitcnt lgkmcnt(0)
	v_mfma_f32_32x32x16_f16 v[2:17], v[40:43], v[120:123], v[2:17]
	ds_read_b128 v[36:39], v195 offset:6144
	ds_read_b128 v[40:43], v195 offset:6656
	s_waitcnt vmcnt(0) lgkmcnt(1)
	v_mfma_f32_32x32x16_f16 v[18:33], v[36:39], v[112:115], v[18:33]
	s_waitcnt lgkmcnt(0)
	v_mfma_f32_32x32x16_f16 v[2:17], v[40:43], v[112:115], v[2:17]
	s_nop 11
	v_max_f32_e32 v1, v19, v18
	v_max3_f32 v37, v20, v21, v3
	v_max3_f32 v1, v1, v2, v4
	v_max3_f32 v36, v37, v24, v25
	v_max3_f32 v1, v1, v5, v22
	v_max3_f32 v36, v36, v8, v9
	v_max3_f32 v1, v1, v23, v6
	v_max3_f32 v36, v36, v28, v29
	v_max3_f32 v1, v1, v7, v26
	v_max3_f32 v36, v36, v12, v13
	v_max3_f32 v1, v1, v27, v10
	v_max3_f32 v36, v36, v32, v33
	v_max3_f32 v1, v1, v11, v30
	v_max3_f32 v36, v36, v16, v17
	v_max3_f32 v1, v1, v31, v14
	v_max3_f32 v1, v1, v15, v36
	v_mov_b32_e32 v36, v1
	s_nop 1
	v_permlane32_swap_b32_e32 v1, v36
	v_max_f32_e32 v194, v36, v1
	v_lshlrev_b32_e32 v1, 1, v0
	v_sub_f32_e32 v36, v2, v194
	v_and_b32_e32 v1, 32, v1
	v_and_b32_e32 v2, 24, v190
	v_lshlrev_b32_e32 v0, 4, v0
	v_add3_u32 v1, 0, v1, v2
	v_and_b32_e32 v0, 0xc0, v0
	v_lshlrev_b32_e32 v2, 8, v46
	v_add3_u32 v192, v1, v2, v0
	v_xor_b32_e32 v0, 0x80000000, v194
	v_sub_f32_e32 v37, v3, v194
	v_sub_f32_e32 v38, v4, v194
	v_sub_f32_e32 v39, v5, v194
	v_sub_f32_e32 v40, v6, v194
	v_sub_f32_e32 v41, v7, v194
	v_sub_f32_e32 v42, v8, v194
	v_sub_f32_e32 v43, v9, v194
	v_sub_f32_e32 v47, v10, v194
	v_sub_f32_e32 v57, v11, v194
	v_sub_f32_e32 v58, v12, v194
	v_sub_f32_e32 v59, v13, v194
	v_sub_f32_e32 v60, v14, v194
	v_sub_f32_e32 v61, v15, v194
	v_mov_b32_e32 v1, v0
	v_mov_b32_e32 v2, v0
	v_mov_b32_e32 v3, v0
	v_mov_b32_e32 v4, v0
	v_mov_b32_e32 v5, v0
	v_mov_b32_e32 v6, v0
	v_mov_b32_e32 v7, v0
	v_mov_b32_e32 v8, v0
	v_mov_b32_e32 v9, v0
	v_mov_b32_e32 v10, v0
	v_mov_b32_e32 v11, v0
	v_mov_b32_e32 v12, v0
	v_mov_b32_e32 v13, v0
	v_mov_b32_e32 v14, v0
	v_mov_b32_e32 v15, v0
	s_waitcnt vmcnt(0) lgkmcnt(0)
	s_barrier
	v_sub_f32_e32 v62, v16, v194
	v_sub_f32_e32 v63, v17, v194
	v_lshl_add_u64 v[16:17], v[44:45], 0, s[12:13]
	s_mov_b32 s1, m0
	s_mov_b32 m0, s25
	s_nop 0
	global_load_lds_dwordx4 v[16:17], off
	s_mov_b32 m0, s1
	s_add_i32 s1, s25, 0xa000
	v_lshl_add_u64 v[16:17], v[34:35], 0, s[2:3]
	s_mov_b32 s11, m0
	s_mov_b32 m0, s1
	s_nop 0
	global_load_lds_dwordx4 v[16:17], off
	s_mov_b32 m0, s11
	ds_read_b128 v[172:175], v195 offset:8192
	ds_read_b128 v[168:171], v195 offset:8704
	ds_read_b128 v[164:167], v195 offset:10240
	ds_read_b128 v[160:163], v195 offset:10752
	ds_read_b128 v[156:159], v195 offset:12288
	ds_read_b128 v[152:155], v195 offset:12800
	ds_read_b128 v[148:151], v195 offset:14336
	ds_read_b128 v[144:147], v195 offset:14848
	s_add_i32 s11, s0, 0
	v_sub_f32_e32 v18, v18, v194
	v_sub_f32_e32 v19, v19, v194
	v_sub_f32_e32 v20, v20, v194
	v_sub_f32_e32 v21, v21, v194
	v_sub_f32_e32 v22, v22, v194
	v_sub_f32_e32 v23, v23, v194
	v_sub_f32_e32 v24, v24, v194
	v_sub_f32_e32 v25, v25, v194
	v_sub_f32_e32 v26, v26, v194
	v_sub_f32_e32 v27, v27, v194
	v_sub_f32_e32 v28, v28, v194
	v_sub_f32_e32 v29, v29, v194
	v_sub_f32_e32 v30, v30, v194
	v_sub_f32_e32 v31, v31, v194
	v_sub_f32_e32 v32, v32, v194
	v_sub_f32_e32 v33, v33, v194
	s_add_u32 s14, s16, s34
	v_exp_f32_e32 v64, v18
	v_exp_f32_e32 v65, v19
	v_exp_f32_e32 v48, v36
	v_exp_f32_e32 v49, v37
	v_exp_f32_e32 v66, v20
	v_exp_f32_e32 v50, v38
	v_exp_f32_e32 v67, v21
	v_exp_f32_e32 v51, v39
	v_exp_f32_e32 v68, v22
	v_exp_f32_e32 v52, v40
	v_exp_f32_e32 v69, v23
	v_exp_f32_e32 v53, v41
	v_exp_f32_e32 v70, v24
	v_exp_f32_e32 v54, v42
	v_exp_f32_e32 v71, v25
	v_exp_f32_e32 v55, v43
	v_exp_f32_e32 v72, v26
	v_exp_f32_e32 v56, v47
	v_exp_f32_e32 v73, v27
	v_exp_f32_e32 v57, v57
	v_exp_f32_e32 v74, v28
	v_exp_f32_e32 v58, v58
	v_exp_f32_e32 v75, v29
	v_exp_f32_e32 v59, v59
	v_exp_f32_e32 v76, v30
	v_exp_f32_e32 v60, v60
	v_exp_f32_e32 v77, v31
	v_exp_f32_e32 v61, v61
	v_exp_f32_e32 v78, v32
	v_exp_f32_e32 v62, v62
	v_exp_f32_e32 v79, v33
	v_exp_f32_e32 v63, v63
	s_addc_u32 s16, s17, s35
	s_waitcnt vmcnt(2) lgkmcnt(0)
	s_barrier
	v_or_b32_e32 v16, s14, v186
	v_mov_b32_e32 v17, s16
	v_lshl_add_u64 v[16:17], v[16:17], 0, s[18:19]
	v_cmp_gt_u32_e64 s[0:1], 32, v188
	s_mov_b32 s16, 0x41000000
	s_mov_b32 s36, 0x43800000
	s_mov_b64 s[4:5], 0x8000
	s_movk_i32 s14, 0x2000
	s_movk_i32 s19, 0x4000
	v_mov_b32_e32 v16, v187
	v_mov_b32_e32 v17, v187
	v_mov_b32_e32 v18, v187
	v_mov_b32_e32 v19, v187
	v_mov_b32_e32 v20, v187
	v_mov_b32_e32 v21, v187
	v_mov_b32_e32 v22, v187
	v_mov_b32_e32 v23, v187
	v_mov_b32_e32 v24, v187
	v_mov_b32_e32 v25, v187
	v_mov_b32_e32 v26, v187
	v_mov_b32_e32 v27, v187
	v_mov_b32_e32 v28, v187
	v_mov_b32_e32 v29, v187
	v_mov_b32_e32 v30, v187
	v_mov_b32_e32 v31, v187
	v_mov_b32_e32 v32, v187
	v_mov_b32_e32 v33, v187
	v_mov_b32_e32 v34, v187
	v_mov_b32_e32 v35, v187
	v_mov_b32_e32 v36, v187
	v_mov_b32_e32 v37, v187
	v_mov_b32_e32 v38, v187
	v_mov_b32_e32 v39, v187
	v_mov_b32_e32 v40, v187
	v_mov_b32_e32 v41, v187
	v_mov_b32_e32 v42, v187
	v_mov_b32_e32 v43, v187
	v_mov_b32_e32 v44, v187
	v_mov_b32_e32 v45, v187
	v_mov_b32_e32 v46, v187
	v_mov_b32_e32 v47, v187
	v_lshl_add_u32 v186, v189, 2, s11
.LBB2_1:
	s_mov_b32 s17, s31
	s_mov_b32 s18, s15
	v_add_u32_e32 v196, s18, v192
	ds_read_b64_tr_b16 v[176:177], v196 offset:24576
	ds_read_b64_tr_b16 v[178:179], v196 offset:25088
	s_waitcnt lgkmcnt(9)
	v_mfma_f32_32x32x16_f16 v[96:111], v[172:175], v[136:139], v[0:15]
	v_add_f32_e32 v80, v64, v65
	v_add_f32_e32 v80, v66, v80
	v_add_f32_e32 v80, v67, v80
	v_add_f32_e32 v80, v68, v80
	v_add_f32_e32 v80, v69, v80
	v_cvt_pk_f16_f32 v140, v64, v65
	v_cvt_pk_f16_f32 v141, v66, v67
	ds_read_b64_tr_b16 v[172:173], v196 offset:28672
	ds_read_b64_tr_b16 v[174:175], v196 offset:29184
	v_add_f32_e32 v64, v70, v80
	s_waitcnt lgkmcnt(10)
	v_mfma_f32_32x32x16_f16 v[80:95], v[168:171], v[136:139], v[0:15]
	v_add_f32_e32 v64, v71, v64
	v_add_f32_e32 v64, v72, v64
	v_add_f32_e32 v64, v73, v64
	v_cvt_pk_f16_f32 v142, v68, v69
	v_cvt_pk_f16_f32 v143, v70, v71
	ds_read_b64_tr_b16 v[68:69], v196 offset:25600
	ds_read_b64_tr_b16 v[70:71], v196 offset:26112
	s_waitcnt lgkmcnt(11)
	v_mfma_f32_32x32x16_f16 v[96:111], v[164:167], v[128:131], v[96:111]
	v_add_f32_e32 v64, v74, v64
	v_add_f32_e32 v64, v75, v64
	v_add_f32_e32 v64, v76, v64
	v_add_f32_e32 v116, v77, v64
	v_cvt_pk_f16_f32 v132, v72, v73
	v_cvt_pk_f16_f32 v133, v74, v75
	ds_read_b64_tr_b16 v[64:65], v196 offset:29696
	ds_read_b64_tr_b16 v[66:67], v196 offset:30208
	s_waitcnt lgkmcnt(12)
	v_mfma_f32_32x32x16_f16 v[80:95], v[160:163], v[128:131], v[80:95]
	v_add_f32_e32 v72, v78, v116
	v_add_f32_e32 v72, v79, v72
	v_add_f32_e32 v72, v48, v72
	v_add_f32_e32 v116, v49, v72
	v_cvt_pk_f16_f32 v134, v76, v77
	v_cvt_pk_f16_f32 v135, v78, v79
	ds_read_b64_tr_b16 v[72:73], v196 offset:26624
	ds_read_b64_tr_b16 v[74:75], v196 offset:27136
	s_waitcnt lgkmcnt(13)
	v_mfma_f32_32x32x16_f16 v[96:111], v[156:159], v[120:123], v[96:111]
	v_add_f32_e32 v76, v50, v116
	v_add_f32_e32 v76, v51, v76
	v_add_f32_e32 v76, v52, v76
	v_add_f32_e32 v76, v53, v76
	v_cvt_pk_f16_f32 v124, v48, v49
	v_cvt_pk_f16_f32 v125, v50, v51
	ds_read_b64_tr_b16 v[48:49], v196 offset:30720
	ds_read_b64_tr_b16 v[50:51], v196 offset:31232
	s_waitcnt lgkmcnt(14)
	v_mfma_f32_32x32x16_f16 v[80:95], v[152:155], v[120:123], v[80:95]
	v_add_f32_e32 v76, v54, v76
	v_add_f32_e32 v76, v55, v76
	v_add_f32_e32 v76, v56, v76
	v_add_f32_e32 v76, v57, v76
	v_cvt_pk_f16_f32 v126, v52, v53
	v_cvt_pk_f16_f32 v127, v54, v55
	ds_read_b64_tr_b16 v[52:53], v196 offset:27648
	ds_read_b64_tr_b16 v[54:55], v196 offset:28160
	s_waitcnt lgkmcnt(14)
	v_mfma_f32_32x32x16_f16 v[96:111], v[148:151], v[112:115], v[96:111]
	v_add_f32_e32 v76, v58, v76
	v_add_f32_e32 v76, v59, v76
	v_add_f32_e32 v76, v60, v76
	v_add_f32_e32 v76, v61, v76
	v_cvt_pk_f16_f32 v116, v56, v57
	v_cvt_pk_f16_f32 v117, v58, v59
	ds_read_b64_tr_b16 v[56:57], v196 offset:31744
	ds_read_b64_tr_b16 v[58:59], v196 offset:32256
	v_mfma_f32_32x32x16_f16 v[80:95], v[144:147], v[112:115], v[80:95]
	v_add_f32_e32 v76, v62, v76
	v_add_f32_e32 v76, v63, v76
	v_cvt_pk_f16_f32 v118, v60, v61
	v_cvt_pk_f16_f32 v119, v62, v63
	s_add_i32 m0, s14, s25
	v_cmp_lt_f32_e32 vcc, s36, v76
	global_load_lds_dwordx4 v180, s[44:45]
	s_add_i32 m0, s28, s26
	s_add_u32 s44, s44, 0x2000
	global_load_lds_dwordx4 v180, s[46:47]
	s_addc_u32 s45, s45, 0
	s_add_u32 s46, s46, 0x2000
	s_addc_u32 s47, s47, 0
	s_cbranch_vccnz .Lmy_rare_1

.LBB2_4:
	v_add_u32_e32 v196, s17, v192
	ds_read_b64_tr_b16 v[144:145], v196 offset:24576
	ds_read_b64_tr_b16 v[146:147], v196 offset:25088
	s_waitcnt lgkmcnt(9)
	v_mfma_f32_32x32x16_f16 v[64:79], v[60:63], v[136:139], v[0:15]
	v_add_f32_e32 v48, v96, v97
	v_add_f32_e32 v48, v98, v48
	v_add_f32_e32 v48, v99, v48
	v_add_f32_e32 v48, v100, v48
	v_add_f32_e32 v48, v101, v48
	v_cvt_pk_f16_f32 v140, v96, v97
	v_cvt_pk_f16_f32 v141, v98, v99
	ds_read_b64_tr_b16 v[152:153], v196 offset:28672
	ds_read_b64_tr_b16 v[154:155], v196 offset:29184
	v_add_f32_e32 v48, v102, v48
	v_add_f32_e32 v48, v103, v48
	v_add_f32_e32 v48, v104, v48
	v_add_f32_e32 v96, v105, v48
	s_waitcnt lgkmcnt(10)
	v_mfma_f32_32x32x16_f16 v[48:63], v[148:151], v[136:139], v[0:15]
	v_cvt_pk_f16_f32 v142, v100, v101
	v_cvt_pk_f16_f32 v143, v102, v103
	ds_read_b64_tr_b16 v[148:149], v196 offset:25600
	ds_read_b64_tr_b16 v[150:151], v196 offset:26112
	s_waitcnt lgkmcnt(11)
	v_mfma_f32_32x32x16_f16 v[64:79], v[176:179], v[128:131], v[64:79]
	v_add_f32_e32 v96, v106, v96
	v_add_f32_e32 v96, v107, v96
	v_add_f32_e32 v96, v108, v96
	v_add_f32_e32 v96, v109, v96
	v_cvt_pk_f16_f32 v132, v104, v105
	v_cvt_pk_f16_f32 v133, v106, v107
	ds_read_b64_tr_b16 v[100:101], v196 offset:29696
	ds_read_b64_tr_b16 v[102:103], v196 offset:30208
	s_waitcnt lgkmcnt(12)
	v_mfma_f32_32x32x16_f16 v[48:63], v[172:175], v[128:131], v[48:63]
	v_add_f32_e32 v96, v110, v96
	v_add_f32_e32 v96, v111, v96
	v_add_f32_e32 v96, v80, v96
	v_add_f32_e32 v104, v81, v96
	v_cvt_pk_f16_f32 v134, v108, v109
	v_cvt_pk_f16_f32 v135, v110, v111
	ds_read_b64_tr_b16 v[96:97], v196 offset:26624
	ds_read_b64_tr_b16 v[98:99], v196 offset:27136
	s_waitcnt lgkmcnt(13)
	v_mfma_f32_32x32x16_f16 v[64:79], v[168:171], v[120:123], v[64:79]
	v_add_f32_e32 v104, v82, v104
	v_add_f32_e32 v104, v83, v104
	v_add_f32_e32 v104, v84, v104
	v_add_f32_e32 v104, v85, v104
	v_cvt_pk_f16_f32 v124, v80, v81
	v_cvt_pk_f16_f32 v125, v82, v83
	ds_read_b64_tr_b16 v[80:81], v196 offset:30720
	ds_read_b64_tr_b16 v[82:83], v196 offset:31232
	s_waitcnt lgkmcnt(14)
	v_mfma_f32_32x32x16_f16 v[48:63], v[164:167], v[120:123], v[48:63]
	v_add_f32_e32 v104, v86, v104
	v_add_f32_e32 v104, v87, v104
	v_add_f32_e32 v104, v88, v104
	v_add_f32_e32 v104, v89, v104
	v_cvt_pk_f16_f32 v126, v84, v85
	v_cvt_pk_f16_f32 v127, v86, v87
	ds_read_b64_tr_b16 v[84:85], v196 offset:27648
	ds_read_b64_tr_b16 v[86:87], v196 offset:28160
	s_waitcnt lgkmcnt(14)
	v_mfma_f32_32x32x16_f16 v[64:79], v[160:163], v[112:115], v[64:79]
	v_add_f32_e32 v104, v90, v104
	v_add_f32_e32 v104, v91, v104
	v_add_f32_e32 v104, v92, v104
	v_add_f32_e32 v104, v93, v104
	v_cvt_pk_f16_f32 v116, v88, v89
	v_cvt_pk_f16_f32 v117, v90, v91
	ds_read_b64_tr_b16 v[88:89], v196 offset:31744
	ds_read_b64_tr_b16 v[90:91], v196 offset:32256
	v_mfma_f32_32x32x16_f16 v[48:63], v[156:159], v[112:115], v[48:63]
	v_add_f32_e32 v104, v94, v104
	v_add_f32_e32 v104, v95, v104
	v_cvt_pk_f16_f32 v118, v92, v93
	v_cvt_pk_f16_f32 v119, v94, v95
	s_add_i32 m0, s19, s25
	v_cmp_lt_f32_e32 vcc, s36, v104
	global_load_lds_dwordx4 v180, s[44:45]
	s_add_i32 m0, s18, s26
	s_add_u32 s44, s44, 0x2000
	global_load_lds_dwordx4 v180, s[46:47]
	s_addc_u32 s45, s45, 0
	s_add_u32 s46, s46, 0x2000
	s_addc_u32 s47, s47, 0
	s_cbranch_vccnz .Lmy_rare_2

.LBB2_5:
	s_add_i32 s14, s19, 0x2000
	s_cmpk_lg_i32 s19, 0x4000
	s_cselect_b32 s14, s14, 0
	s_waitcnt lgkmcnt(14)
	v_mfma_f32_32x32x16_f16 v[16:31], v[140:143], v[144:147], v[16:31]
	v_exp_f32_e32 v64, v64
	v_exp_f32_e32 v65, v65
	v_exp_f32_e32 v66, v66
	v_exp_f32_e32 v67, v67
	s_waitcnt lgkmcnt(12)
	v_mfma_f32_32x32x16_f16 v[32:47], v[140:143], v[152:155], v[32:47]
	v_exp_f32_e32 v68, v68
	v_exp_f32_e32 v69, v69
	v_exp_f32_e32 v70, v70
	v_exp_f32_e32 v71, v71
	v_add_u32_e32 v92, s14, v195
	ds_read_b128 v[172:175], v92
	ds_read_b128 v[168:171], v92 offset:512
	s_waitcnt lgkmcnt(12)
	v_mfma_f32_32x32x16_f16 v[16:31], v[132:135], v[148:151], v[16:31]
	v_exp_f32_e32 v72, v72
	v_exp_f32_e32 v73, v73
	v_exp_f32_e32 v74, v74
	v_exp_f32_e32 v75, v75
	ds_read_b128 v[164:167], v92 offset:2048
	ds_read_b128 v[160:163], v92 offset:2560
	s_waitcnt lgkmcnt(12)
	v_mfma_f32_32x32x16_f16 v[32:47], v[132:135], v[100:103], v[32:47]
	v_exp_f32_e32 v76, v76
	v_exp_f32_e32 v77, v77
	v_exp_f32_e32 v78, v78
	v_exp_f32_e32 v79, v79
	ds_read_b128 v[156:159], v92 offset:4096
	ds_read_b128 v[152:155], v92 offset:4608
	s_waitcnt lgkmcnt(12)
	v_mfma_f32_32x32x16_f16 v[16:31], v[124:127], v[96:99], v[16:31]
	v_exp_f32_e32 v48, v48
	v_exp_f32_e32 v49, v49
	v_exp_f32_e32 v50, v50
	v_exp_f32_e32 v51, v51
	ds_read_b128 v[148:151], v92 offset:6144
	ds_read_b128 v[144:147], v92 offset:6656
	s_waitcnt lgkmcnt(12)
	v_mfma_f32_32x32x16_f16 v[32:47], v[124:127], v[80:83], v[32:47]
	v_exp_f32_e32 v52, v52
	v_exp_f32_e32 v53, v53
	v_exp_f32_e32 v54, v54
	v_exp_f32_e32 v55, v55
	s_waitcnt lgkmcnt(10)
	v_mfma_f32_32x32x16_f16 v[16:31], v[116:119], v[84:87], v[16:31]
	v_exp_f32_e32 v56, v56
	v_exp_f32_e32 v57, v57
	v_exp_f32_e32 v58, v58
	v_exp_f32_e32 v59, v59
	s_waitcnt lgkmcnt(8)
	v_mfma_f32_32x32x16_f16 v[32:47], v[116:119], v[88:91], v[32:47]
	v_exp_f32_e32 v60, v60
	v_exp_f32_e32 v61, v61
	v_exp_f32_e32 v62, v62
	v_exp_f32_e32 v63, v63
	s_add_i32 s6, s14, 0x2000
	s_cmpk_lg_i32 s14, 0x4000
	s_cselect_b32 s19, s6, 0
	s_add_i32 s27, s27, 2
	s_mov_b32 s15, s29
	s_mov_b32 s31, s28
	s_mov_b32 s29, s18
	s_mov_b32 s28, s17
	s_cmp_gt_u32 s27, 28
	s_waitcnt vmcnt(3) lgkmcnt(0)
	s_barrier
	s_cbranch_scc0 .LBB2_1

.Lmy_rare_1:
	s_sub_u32 s38, s44, s25
	s_subb_u32 s39, s45, 0
	s_sub_u32 s38, s38, 0xa000
	s_subb_u32 s39, s39, 0
	s_add_u32 s48, s38, 0x1000
	s_addc_u32 s49, s39, 0
	v_lshlrev_b32_e32 v160, 4, v189
	v_lshl_add_u32 v160, v191, 1, v160
	v_xor_b32_e32 v166, 0x80000000, v194
	s_lshl_b32 s42, s23, 12
	v_lshlrev_b32_e32 v167, 2, v188
	v_add_u32_e32 v167, s42, v167
	global_load_dwordx4 v[140:143], v160, s[38:39]
	global_load_dwordx4 v[132:135], v160, s[38:39] offset:2048
	global_load_dwordx4 v[124:127], v160, s[48:49]
	global_load_dwordx4 v[116:119], v160, s[48:49] offset:2048
	v_mov_b32_e32 v144, v166
	v_mov_b32_e32 v145, v166
	v_mov_b32_e32 v146, v166
	v_mov_b32_e32 v147, v166
	v_mov_b32_e32 v148, v166
	v_mov_b32_e32 v149, v166
	v_mov_b32_e32 v150, v166
	v_mov_b32_e32 v151, v166
	v_mov_b32_e32 v152, v166
	v_mov_b32_e32 v153, v166
	v_mov_b32_e32 v154, v166
	v_mov_b32_e32 v155, v166
	v_mov_b32_e32 v156, v166
	v_mov_b32_e32 v157, v166
	v_mov_b32_e32 v158, v166
	v_mov_b32_e32 v159, v166
	s_waitcnt vmcnt(0)
	s_nop 1
	v_mfma_f32_32x32x16_f16 v[144:159], v[140:143], v[136:139], v[144:159]
	v_mfma_f32_32x32x16_f16 v[144:159], v[132:135], v[128:131], v[144:159]
	v_mfma_f32_32x32x16_f16 v[144:159], v[124:127], v[120:123], v[144:159]
	v_mfma_f32_32x32x16_f16 v[144:159], v[116:119], v[112:115], v[144:159]
	s_nop 15
	s_nop 3
	v_max3_f32 v164, v144, v145, v146
	v_max3_f32 v164, v164, v147, v148
	v_max3_f32 v164, v164, v149, v150
	v_max3_f32 v164, v164, v151, v152
	v_max3_f32 v164, v164, v153, v154
	v_max3_f32 v164, v164, v155, v156
	v_max3_f32 v164, v164, v157, v158
	v_max_f32_e32 v164, v164, v159
	ds_write_b32 v167, v144 offset:59392
	ds_write_b32 v167, v145 offset:59648
	ds_write_b32 v167, v146 offset:59904
	ds_write_b32 v167, v147 offset:60160
	ds_write_b32 v167, v148 offset:60416
	ds_write_b32 v167, v149 offset:60672
	ds_write_b32 v167, v150 offset:60928
	ds_write_b32 v167, v151 offset:61184
	ds_write_b32 v167, v152 offset:61440
	ds_write_b32 v167, v153 offset:61696
	ds_write_b32 v167, v154 offset:61952
	ds_write_b32 v167, v155 offset:62208
	ds_write_b32 v167, v156 offset:62464
	ds_write_b32 v167, v157 offset:62720
	ds_write_b32 v167, v158 offset:62976
	ds_write_b32 v167, v159 offset:63232
	s_waitcnt lgkmcnt(0)
	global_load_dwordx4 v[140:143], v160, s[38:39] offset:512
	global_load_dwordx4 v[132:135], v160, s[38:39] offset:2560
	global_load_dwordx4 v[124:127], v160, s[48:49] offset:512
	global_load_dwordx4 v[116:119], v160, s[48:49] offset:2560
	v_mov_b32_e32 v144, v166
	v_mov_b32_e32 v145, v166
	v_mov_b32_e32 v146, v166
	v_mov_b32_e32 v147, v166
	v_mov_b32_e32 v148, v166
	v_mov_b32_e32 v149, v166
	v_mov_b32_e32 v150, v166
	v_mov_b32_e32 v151, v166
	v_mov_b32_e32 v152, v166
	v_mov_b32_e32 v153, v166
	v_mov_b32_e32 v154, v166
	v_mov_b32_e32 v155, v166
	v_mov_b32_e32 v156, v166
	v_mov_b32_e32 v157, v166
	v_mov_b32_e32 v158, v166
	v_mov_b32_e32 v159, v166
	s_waitcnt vmcnt(0)
	s_nop 1
	v_mfma_f32_32x32x16_f16 v[144:159], v[140:143], v[136:139], v[144:159]
	v_mfma_f32_32x32x16_f16 v[144:159], v[132:135], v[128:131], v[144:159]
	v_mfma_f32_32x32x16_f16 v[144:159], v[124:127], v[120:123], v[144:159]
	v_mfma_f32_32x32x16_f16 v[144:159], v[116:119], v[112:115], v[144:159]
	s_nop 15
	s_nop 3
	v_max3_f32 v165, v144, v145, v146
	v_max3_f32 v165, v165, v147, v148
	v_max3_f32 v165, v165, v149, v150
	v_max3_f32 v165, v165, v151, v152
	v_max3_f32 v165, v165, v153, v154
	v_max3_f32 v165, v165, v155, v156
	v_max3_f32 v165, v165, v157, v158
	v_max_f32_e32 v165, v165, v159
	v_max_f32_e32 v164, v164, v165
	v_mov_b32_e32 v165, v164
	s_nop 1
	v_permlane32_swap_b32_e32 v164, v165
	v_max_f32_e32 v164, v165, v164
	s_mov_b32 s37, 0x41000000
	v_cmp_lt_f32_e32 vcc, s37, v164
	v_max_f32_e32 v164, 0, v164
	s_nop 4
	s_cbranch_vccnz .Lmy_rare_1_rs
	v_mov_b32_e32 v164, 0
	s_branch .Lmy_rare_1_nr

.Lmy_rare_2:
	s_sub_u32 s38, s44, s25
	s_subb_u32 s39, s45, 0
	s_sub_u32 s38, s38, 0xa000
	s_subb_u32 s39, s39, 0
	s_add_u32 s48, s38, 0x1000
	s_addc_u32 s49, s39, 0
	v_lshlrev_b32_e32 v172, 4, v189
	v_lshl_add_u32 v172, v191, 1, v172
	v_xor_b32_e32 v178, 0x80000000, v194
	s_lshl_b32 s42, s23, 12
	v_lshlrev_b32_e32 v179, 2, v188
	v_add_u32_e32 v179, s42, v179
	global_load_dwordx4 v[140:143], v172, s[38:39]
	global_load_dwordx4 v[132:135], v172, s[38:39] offset:2048
	global_load_dwordx4 v[124:127], v172, s[48:49]
	global_load_dwordx4 v[116:119], v172, s[48:49] offset:2048
	v_mov_b32_e32 v156, v178
	v_mov_b32_e32 v157, v178
	v_mov_b32_e32 v158, v178
	v_mov_b32_e32 v159, v178
	v_mov_b32_e32 v160, v178
	v_mov_b32_e32 v161, v178
	v_mov_b32_e32 v162, v178
	v_mov_b32_e32 v163, v178
	v_mov_b32_e32 v164, v178
	v_mov_b32_e32 v165, v178
	v_mov_b32_e32 v166, v178
	v_mov_b32_e32 v167, v178
	v_mov_b32_e32 v168, v178
	v_mov_b32_e32 v169, v178
	v_mov_b32_e32 v170, v178
	v_mov_b32_e32 v171, v178
	s_waitcnt vmcnt(0)
	s_nop 1
	v_mfma_f32_32x32x16_f16 v[156:171], v[140:143], v[136:139], v[156:171]
	v_mfma_f32_32x32x16_f16 v[156:171], v[132:135], v[128:131], v[156:171]
	v_mfma_f32_32x32x16_f16 v[156:171], v[124:127], v[120:123], v[156:171]
	v_mfma_f32_32x32x16_f16 v[156:171], v[116:119], v[112:115], v[156:171]
	s_nop 15
	s_nop 3
	v_max3_f32 v176, v156, v157, v158
	v_max3_f32 v176, v176, v159, v160
	v_max3_f32 v176, v176, v161, v162
	v_max3_f32 v176, v176, v163, v164
	v_max3_f32 v176, v176, v165, v166
	v_max3_f32 v176, v176, v167, v168
	v_max3_f32 v176, v176, v169, v170
	v_max_f32_e32 v176, v176, v171
	ds_write_b32 v179, v156 offset:59392
	ds_write_b32 v179, v157 offset:59648
	ds_write_b32 v179, v158 offset:59904
	ds_write_b32 v179, v159 offset:60160
	ds_write_b32 v179, v160 offset:60416
	ds_write_b32 v179, v161 offset:60672
	ds_write_b32 v179, v162 offset:60928
	ds_write_b32 v179, v163 offset:61184
	ds_write_b32 v179, v164 offset:61440
	ds_write_b32 v179, v165 offset:61696
	ds_write_b32 v179, v166 offset:61952
	ds_write_b32 v179, v167 offset:62208
	ds_write_b32 v179, v168 offset:62464
	ds_write_b32 v179, v169 offset:62720
	ds_write_b32 v179, v170 offset:62976
	ds_write_b32 v179, v171 offset:63232
	s_waitcnt lgkmcnt(0)
	global_load_dwordx4 v[140:143], v172, s[38:39] offset:512
	global_load_dwordx4 v[132:135], v172, s[38:39] offset:2560
	global_load_dwordx4 v[124:127], v172, s[48:49] offset:512
	global_load_dwordx4 v[116:119], v172, s[48:49] offset:2560
	v_mov_b32_e32 v156, v178
	v_mov_b32_e32 v157, v178
	v_mov_b32_e32 v158, v178
	v_mov_b32_e32 v159, v178
	v_mov_b32_e32 v160, v178
	v_mov_b32_e32 v161, v178
	v_mov_b32_e32 v162, v178
	v_mov_b32_e32 v163, v178
	v_mov_b32_e32 v164, v178
	v_mov_b32_e32 v165, v178
	v_mov_b32_e32 v166, v178
	v_mov_b32_e32 v167, v178
	v_mov_b32_e32 v168, v178
	v_mov_b32_e32 v169, v178
	v_mov_b32_e32 v170, v178
	v_mov_b32_e32 v171, v178
	s_waitcnt vmcnt(0)
	s_nop 1
	v_mfma_f32_32x32x16_f16 v[156:171], v[140:143], v[136:139], v[156:171]
	v_mfma_f32_32x32x16_f16 v[156:171], v[132:135], v[128:131], v[156:171]
	v_mfma_f32_32x32x16_f16 v[156:171], v[124:127], v[120:123], v[156:171]
	v_mfma_f32_32x32x16_f16 v[156:171], v[116:119], v[112:115], v[156:171]
	s_nop 15
	s_nop 3
	v_max3_f32 v177, v156, v157, v158
	v_max3_f32 v177, v177, v159, v160
	v_max3_f32 v177, v177, v161, v162
	v_max3_f32 v177, v177, v163, v164
	v_max3_f32 v177, v177, v165, v166
	v_max3_f32 v177, v177, v167, v168
	v_max3_f32 v177, v177, v169, v170
	v_max_f32_e32 v177, v177, v171
	v_max_f32_e32 v176, v176, v177
	v_mov_b32_e32 v177, v176
	s_nop 1
	v_permlane32_swap_b32_e32 v176, v177
	v_max_f32_e32 v176, v177, v176
	s_mov_b32 s37, 0x41000000
	v_cmp_lt_f32_e32 vcc, s37, v176
	v_max_f32_e32 v176, 0, v176
	s_nop 4
	s_cbranch_vccnz .Lmy_rare_2_rs
	v_mov_b32_e32 v176, 0
	s_branch .Lmy_rare_2_nr

.Lmy_rare_3:
	s_sub_u32 s38, s44, s25
	s_subb_u32 s39, s45, 0
	s_sub_u32 s38, s38, 0x8000
	s_subb_u32 s39, s39, 0
	s_add_u32 s48, s38, 0x1000
	s_addc_u32 s49, s39, 0
	v_lshlrev_b32_e32 v160, 4, v189
	v_lshl_add_u32 v160, v191, 1, v160
	v_xor_b32_e32 v166, 0x80000000, v194
	s_lshl_b32 s42, s23, 12
	v_lshlrev_b32_e32 v167, 2, v188
	v_add_u32_e32 v167, s42, v167
	global_load_dwordx4 v[140:143], v160, s[38:39]
	global_load_dwordx4 v[132:135], v160, s[38:39] offset:2048
	global_load_dwordx4 v[124:127], v160, s[48:49]
	global_load_dwordx4 v[116:119], v160, s[48:49] offset:2048
	v_mov_b32_e32 v144, v166
	v_mov_b32_e32 v145, v166
	v_mov_b32_e32 v146, v166
	v_mov_b32_e32 v147, v166
	v_mov_b32_e32 v148, v166
	v_mov_b32_e32 v149, v166
	v_mov_b32_e32 v150, v166
	v_mov_b32_e32 v151, v166
	v_mov_b32_e32 v152, v166
	v_mov_b32_e32 v153, v166
	v_mov_b32_e32 v154, v166
	v_mov_b32_e32 v155, v166
	v_mov_b32_e32 v156, v166
	v_mov_b32_e32 v157, v166
	v_mov_b32_e32 v158, v166
	v_mov_b32_e32 v159, v166
	s_waitcnt vmcnt(0)
	s_nop 1
	v_mfma_f32_32x32x16_f16 v[144:159], v[140:143], v[136:139], v[144:159]
	v_mfma_f32_32x32x16_f16 v[144:159], v[132:135], v[128:131], v[144:159]
	v_mfma_f32_32x32x16_f16 v[144:159], v[124:127], v[120:123], v[144:159]
	v_mfma_f32_32x32x16_f16 v[144:159], v[116:119], v[112:115], v[144:159]
	s_nop 15
	s_nop 3
	v_max3_f32 v164, v144, v145, v146
	v_max3_f32 v164, v164, v147, v148
	v_max3_f32 v164, v164, v149, v150
	v_max3_f32 v164, v164, v151, v152
	v_max3_f32 v164, v164, v153, v154
	v_max3_f32 v164, v164, v155, v156
	v_max3_f32 v164, v164, v157, v158
	v_max_f32_e32 v164, v164, v159
	ds_write_b32 v167, v144 offset:59392
	ds_write_b32 v167, v145 offset:59648
	ds_write_b32 v167, v146 offset:59904
	ds_write_b32 v167, v147 offset:60160
	ds_write_b32 v167, v148 offset:60416
	ds_write_b32 v167, v149 offset:60672
	ds_write_b32 v167, v150 offset:60928
	ds_write_b32 v167, v151 offset:61184
	ds_write_b32 v167, v152 offset:61440
	ds_write_b32 v167, v153 offset:61696
	ds_write_b32 v167, v154 offset:61952
	ds_write_b32 v167, v155 offset:62208
	ds_write_b32 v167, v156 offset:62464
	ds_write_b32 v167, v157 offset:62720
	ds_write_b32 v167, v158 offset:62976
	ds_write_b32 v167, v159 offset:63232
	s_waitcnt lgkmcnt(0)
	global_load_dwordx4 v[140:143], v160, s[38:39] offset:512
	global_load_dwordx4 v[132:135], v160, s[38:39] offset:2560
	global_load_dwordx4 v[124:127], v160, s[48:49] offset:512
	global_load_dwordx4 v[116:119], v160, s[48:49] offset:2560
	v_mov_b32_e32 v144, v166
	v_mov_b32_e32 v145, v166
	v_mov_b32_e32 v146, v166
	v_mov_b32_e32 v147, v166
	v_mov_b32_e32 v148, v166
	v_mov_b32_e32 v149, v166
	v_mov_b32_e32 v150, v166
	v_mov_b32_e32 v151, v166
	v_mov_b32_e32 v152, v166
	v_mov_b32_e32 v153, v166
	v_mov_b32_e32 v154, v166
	v_mov_b32_e32 v155, v166
	v_mov_b32_e32 v156, v166
	v_mov_b32_e32 v157, v166
	v_mov_b32_e32 v158, v166
	v_mov_b32_e32 v159, v166
	s_waitcnt vmcnt(0)
	s_nop 1
	v_mfma_f32_32x32x16_f16 v[144:159], v[140:143], v[136:139], v[144:159]
	v_mfma_f32_32x32x16_f16 v[144:159], v[132:135], v[128:131], v[144:159]
	v_mfma_f32_32x32x16_f16 v[144:159], v[124:127], v[120:123], v[144:159]
	v_mfma_f32_32x32x16_f16 v[144:159], v[116:119], v[112:115], v[144:159]
	s_nop 15
	s_nop 3
	v_max3_f32 v165, v144, v145, v146
	v_max3_f32 v165, v165, v147, v148
	v_max3_f32 v165, v165, v149, v150
	v_max3_f32 v165, v165, v151, v152
	v_max3_f32 v165, v165, v153, v154
	v_max3_f32 v165, v165, v155, v156
	v_max3_f32 v165, v165, v157, v158
	v_max_f32_e32 v165, v165, v159
	v_max_f32_e32 v164, v164, v165
	v_mov_b32_e32 v165, v164
	s_nop 1
	v_permlane32_swap_b32_e32 v164, v165
	v_max_f32_e32 v164, v165, v164
	s_mov_b32 s37, 0x41000000
	v_cmp_lt_f32_e32 vcc, s37, v164
	v_max_f32_e32 v164, 0, v164
	s_nop 4
	s_cbranch_vccnz .Lmy_rare_3_rs
	v_mov_b32_e32 v164, 0
	s_branch .Lmy_rare_3_nr

.Lmy_rare_4:
	s_sub_u32 s38, s44, s25
	s_subb_u32 s39, s45, 0
	s_sub_u32 s38, s38, 0x6000
	s_subb_u32 s39, s39, 0
	s_add_u32 s48, s38, 0x1000
	s_addc_u32 s49, s39, 0
	v_lshlrev_b32_e32 v160, 4, v189
	v_lshl_add_u32 v160, v191, 1, v160
	v_xor_b32_e32 v166, 0x80000000, v194
	s_lshl_b32 s42, s23, 12
	v_lshlrev_b32_e32 v167, 2, v188
	v_add_u32_e32 v167, s42, v167
	global_load_dwordx4 v[140:143], v160, s[38:39]
	global_load_dwordx4 v[132:135], v160, s[38:39] offset:2048
	global_load_dwordx4 v[124:127], v160, s[48:49]
	global_load_dwordx4 v[116:119], v160, s[48:49] offset:2048
	v_mov_b32_e32 v144, v166
	v_mov_b32_e32 v145, v166
	v_mov_b32_e32 v146, v166
	v_mov_b32_e32 v147, v166
	v_mov_b32_e32 v148, v166
	v_mov_b32_e32 v149, v166
	v_mov_b32_e32 v150, v166
	v_mov_b32_e32 v151, v166
	v_mov_b32_e32 v152, v166
	v_mov_b32_e32 v153, v166
	v_mov_b32_e32 v154, v166
	v_mov_b32_e32 v155, v166
	v_mov_b32_e32 v156, v166
	v_mov_b32_e32 v157, v166
	v_mov_b32_e32 v158, v166
	v_mov_b32_e32 v159, v166
	s_waitcnt vmcnt(0)
	s_nop 1
	v_mfma_f32_32x32x16_f16 v[144:159], v[140:143], v[136:139], v[144:159]
	v_mfma_f32_32x32x16_f16 v[144:159], v[132:135], v[128:131], v[144:159]
	v_mfma_f32_32x32x16_f16 v[144:159], v[124:127], v[120:123], v[144:159]
	v_mfma_f32_32x32x16_f16 v[144:159], v[116:119], v[112:115], v[144:159]
	s_nop 15
	s_nop 3
	v_max3_f32 v164, v144, v145, v146
	v_max3_f32 v164, v164, v147, v148
	v_max3_f32 v164, v164, v149, v150
	v_max3_f32 v164, v164, v151, v152
	v_max3_f32 v164, v164, v153, v154
	v_max3_f32 v164, v164, v155, v156
	v_max3_f32 v164, v164, v157, v158
	v_max_f32_e32 v164, v164, v159
	ds_write_b32 v167, v144 offset:59392
	ds_write_b32 v167, v145 offset:59648
	ds_write_b32 v167, v146 offset:59904
	ds_write_b32 v167, v147 offset:60160
	ds_write_b32 v167, v148 offset:60416
	ds_write_b32 v167, v149 offset:60672
	ds_write_b32 v167, v150 offset:60928
	ds_write_b32 v167, v151 offset:61184
	ds_write_b32 v167, v152 offset:61440
	ds_write_b32 v167, v153 offset:61696
	ds_write_b32 v167, v154 offset:61952
	ds_write_b32 v167, v155 offset:62208
	ds_write_b32 v167, v156 offset:62464
	ds_write_b32 v167, v157 offset:62720
	ds_write_b32 v167, v158 offset:62976
	ds_write_b32 v167, v159 offset:63232
	s_waitcnt lgkmcnt(0)
	global_load_dwordx4 v[140:143], v160, s[38:39] offset:512
	global_load_dwordx4 v[132:135], v160, s[38:39] offset:2560
	global_load_dwordx4 v[124:127], v160, s[48:49] offset:512
	global_load_dwordx4 v[116:119], v160, s[48:49] offset:2560
	v_mov_b32_e32 v144, v166
	v_mov_b32_e32 v145, v166
	v_mov_b32_e32 v146, v166
	v_mov_b32_e32 v147, v166
	v_mov_b32_e32 v148, v166
	v_mov_b32_e32 v149, v166
	v_mov_b32_e32 v150, v166
	v_mov_b32_e32 v151, v166
	v_mov_b32_e32 v152, v166
	v_mov_b32_e32 v153, v166
	v_mov_b32_e32 v154, v166
	v_mov_b32_e32 v155, v166
	v_mov_b32_e32 v156, v166
	v_mov_b32_e32 v157, v166
	v_mov_b32_e32 v158, v166
	v_mov_b32_e32 v159, v166
	s_waitcnt vmcnt(0)
	s_nop 1
	v_mfma_f32_32x32x16_f16 v[144:159], v[140:143], v[136:139], v[144:159]
	v_mfma_f32_32x32x16_f16 v[144:159], v[132:135], v[128:131], v[144:159]
	v_mfma_f32_32x32x16_f16 v[144:159], v[124:127], v[120:123], v[144:159]
	v_mfma_f32_32x32x16_f16 v[144:159], v[116:119], v[112:115], v[144:159]
	s_nop 15
	s_nop 3
	v_max3_f32 v165, v144, v145, v146
	v_max3_f32 v165, v165, v147, v148
	v_max3_f32 v165, v165, v149, v150
	v_max3_f32 v165, v165, v151, v152
	v_max3_f32 v165, v165, v153, v154
	v_max3_f32 v165, v165, v155, v156
	v_max3_f32 v165, v165, v157, v158
	v_max_f32_e32 v165, v165, v159
	v_max_f32_e32 v164, v164, v165
	v_mov_b32_e32 v165, v164
	s_nop 1
	v_permlane32_swap_b32_e32 v164, v165
	v_max_f32_e32 v164, v165, v164
	s_mov_b32 s37, 0x41000000
	v_cmp_lt_f32_e32 vcc, s37, v164
	v_max_f32_e32 v164, 0, v164
	s_nop 4
	s_cbranch_vccnz .Lmy_rare_4_rs
	v_mov_b32_e32 v164, 0
	s_branch .Lmy_rare_4_nr

	.amdhsa_kernel _Z11attn_kernelPKDF16_S0_PDF16_
		.amdhsa_group_segment_fixed_size 0
		.amdhsa_private_segment_fixed_size 0
		.amdhsa_kernarg_size 24
		.amdhsa_user_sgpr_count 2
		.amdhsa_user_sgpr_dispatch_ptr 0
		.amdhsa_user_sgpr_queue_ptr 0
		.amdhsa_user_sgpr_kernarg_segment_ptr 1
		.amdhsa_user_sgpr_dispatch_id 0
		.amdhsa_user_sgpr_kernarg_preload_length 0
		.amdhsa_user_sgpr_kernarg_preload_offset 0
		.amdhsa_user_sgpr_private_segment_size 0
		.amdhsa_uses_dynamic_stack 0
		.amdhsa_enable_private_segment 0
		.amdhsa_system_sgpr_workgroup_id_x 1
		.amdhsa_system_sgpr_workgroup_id_y 0
		.amdhsa_system_sgpr_workgroup_id_z 0
		.amdhsa_system_sgpr_workgroup_info 0
		.amdhsa_system_vgpr_workitem_id 0
		.amdhsa_next_free_vgpr 199
		.amdhsa_next_free_sgpr 50
		.amdhsa_accum_offset 200
		.amdhsa_reserve_vcc 1
		.amdhsa_float_round_mode_32 0
		.amdhsa_float_round_mode_16_64 0
		.amdhsa_float_denorm_mode_32 3
		.amdhsa_float_denorm_mode_16_64 3
		.amdhsa_dx10_clamp 1
		.amdhsa_ieee_mode 1
		.amdhsa_fp16_overflow 0
		.amdhsa_tg_split 0
		.amdhsa_exception_fp_ieee_invalid_op 0
		.amdhsa_exception_fp_denorm_src 0
		.amdhsa_exception_fp_ieee_div_zero 0
		.amdhsa_exception_fp_ieee_overflow 0
		.amdhsa_exception_fp_ieee_underflow 0
		.amdhsa_exception_fp_ieee_inexact 0
		.amdhsa_exception_int_div_zero 0
	.end_amdhsa_kernel

amdhsa.kernels:
  - .agpr_count:     0
    .args:
      - .actual_access:  read_only
        .address_space:  global
        .offset:         0
        .size:           8
        .value_kind:     global_buffer
      - .actual_access:  read_only
        .address_space:  global
        .offset:         8
        .size:           8
        .value_kind:     global_buffer
      - .actual_access:  read_only
        .address_space:  global
        .offset:         16
        .size:           8
        .value_kind:     global_buffer
      - .actual_access:  read_only
        .address_space:  global
        .offset:         24
        .size:           8
        .value_kind:     global_buffer
      - .actual_access:  read_only
        .address_space:  global
        .offset:         32
        .size:           8
        .value_kind:     global_buffer
      - .actual_access:  write_only
        .address_space:  global
        .offset:         40
        .size:           8
        .value_kind:     global_buffer
      - .actual_access:  write_only
        .address_space:  global
        .offset:         48
        .size:           8
        .value_kind:     global_buffer
      - .actual_access:  write_only
        .address_space:  global
        .offset:         56
        .size:           8
        .value_kind:     global_buffer
      - .actual_access:  write_only
        .address_space:  global
        .offset:         64
        .size:           8
        .value_kind:     global_buffer
    .group_segment_fixed_size: 0
    .kernarg_segment_align: 8
    .kernarg_segment_size: 72
    .language:       OpenCL C
    .language_version:
      - 2
      - 0
    .max_flat_workgroup_size: 256
    .name:           _Z11prep_kernelPKfS0_S0_S0_S0_PDF16_S1_S1_S1_
    .private_segment_fixed_size: 0
    .sgpr_count:     21
    .sgpr_spill_count: 0
    .symbol:         _Z11prep_kernelPKfS0_S0_S0_S0_PDF16_S1_S1_S1_.kd
    .uniform_work_group_size: 1
    .uses_dynamic_stack: false
    .vgpr_count:     18
    .vgpr_spill_count: 0
    .wavefront_size: 64
  - .agpr_count:     0
    .args:
      - .actual_access:  read_only
        .address_space:  global
        .offset:         0
        .size:           8
        .value_kind:     global_buffer
      - .actual_access:  read_only
        .address_space:  global
        .offset:         8
        .size:           8
        .value_kind:     global_buffer
      - .actual_access:  read_only
        .address_space:  global
        .offset:         16
        .size:           8
        .value_kind:     global_buffer
      - .actual_access:  read_only
        .address_space:  global
        .offset:         24
        .size:           8
        .value_kind:     global_buffer
      - .actual_access:  read_only
        .address_space:  global
        .offset:         32
        .size:           8
        .value_kind:     global_buffer
      - .actual_access:  write_only
        .address_space:  global
        .offset:         40
        .size:           8
        .value_kind:     global_buffer
      - .actual_access:  write_only
        .address_space:  global
        .offset:         48
        .size:           8
        .value_kind:     global_buffer
    .group_segment_fixed_size: 0
    .kernarg_segment_align: 8
    .kernarg_segment_size: 56
    .language:       OpenCL C
    .language_version:
      - 2
      - 0
    .max_flat_workgroup_size: 512
    .name:           _Z11proj_kernelPKfS0_PKDF16_S0_S0_PDF16_S3_
    .private_segment_fixed_size: 0
    .sgpr_count:     21
    .sgpr_spill_count: 0
    .symbol:         _Z11proj_kernelPKfS0_PKDF16_S0_S0_PDF16_S3_.kd
    .uniform_work_group_size: 1
    .uses_dynamic_stack: false
    .vgpr_count:     170
    .vgpr_spill_count: 0
    .wavefront_size: 64
  - .agpr_count:     0
    .args:
      - .address_space:  global
        .offset:         0
        .size:           8
        .value_kind:     global_buffer
      - .address_space:  global
        .offset:         8
        .size:           8
        .value_kind:     global_buffer
      - .actual_access:  write_only
        .address_space:  global
        .offset:         16
        .size:           8
        .value_kind:     global_buffer
    .group_segment_fixed_size: 0
    .kernarg_segment_align: 8
    .kernarg_segment_size: 24
    .language:       OpenCL C
    .language_version:
      - 2
      - 0
    .max_flat_workgroup_size: 512
    .name:           _Z11attn_kernelPKDF16_S0_PDF16_
    .private_segment_fixed_size: 0
    .sgpr_count:     56
    .sgpr_spill_count: 0
    .symbol:         _Z11attn_kernelPKDF16_S0_PDF16_.kd
    .uniform_work_group_size: 1
    .uses_dynamic_stack: false
    .vgpr_count:     199
    .vgpr_spill_count: 0
    .wavefront_size: 64
  - .agpr_count:     0
    .args:
      - .actual_access:  read_only
        .address_space:  global
        .offset:         0
        .size:           8
        .value_kind:     global_buffer
      - .actual_access:  read_only
        .address_space:  global
        .offset:         8
        .size:           8
        .value_kind:     global_buffer
      - .actual_access:  read_only
        .address_space:  global
        .offset:         16
        .size:           8
        .value_kind:     global_buffer
      - .actual_access:  read_only
        .address_space:  global
        .offset:         24
        .size:           8
        .value_kind:     global_buffer
      - .actual_access:  read_only
        .address_space:  global
        .offset:         32
        .size:           8
        .value_kind:     global_buffer
      - .address_space:  global
        .offset:         40
        .size:           8
        .value_kind:     global_buffer
      - .actual_access:  read_only
        .address_space:  global
        .offset:         48
        .size:           8
        .value_kind:     global_buffer
      - .actual_access:  read_only
        .address_space:  global
        .offset:         56
        .size:           8
        .value_kind:     global_buffer
      - .actual_access:  read_only
        .address_space:  global
        .offset:         64
        .size:           8
        .value_kind:     global_buffer
      - .address_space:  global
        .offset:         72
        .size:           8
        .value_kind:     global_buffer
      - .actual_access:  read_only
        .address_space:  global
        .offset:         80
        .size:           8
        .value_kind:     global_buffer
      - .actual_access:  write_only
        .address_space:  global
        .offset:         88
        .size:           8
        .value_kind:     global_buffer
    .group_segment_fixed_size: 0
    .kernarg_segment_align: 8
    .kernarg_segment_size: 96
    .language:       OpenCL C
    .language_version:
      - 2
      - 0
    .max_flat_workgroup_size: 512
    .name:           _Z10ffn_kernelPKfS0_PKDF16_S2_S0_S2_S0_S0_S0_S2_S0_Pf
    .private_segment_fixed_size: 0
    .sgpr_count:     24
    .sgpr_spill_count: 0
    .symbol:         _Z10ffn_kernelPKfS0_PKDF16_S2_S0_S2_S0_S0_S0_S2_S0_Pf.kd
    .uniform_work_group_size: 1
    .uses_dynamic_stack: false
    .vgpr_count:     230
    .vgpr_spill_count: 0
    .wavefront_size: 64
